# MoE gate/up GEMM: next tile's gathered row-index wait and offset arithmetic moved behind the accumulator zeroing instead of right after the gather loads
# speedup vs baseline: 1.0007x; 1.0007x over previous
;     __device__ __forceinline__ void a_offsets(const Unit& u, const int (&Rr)[2], const int (&Cc)[2], unsigned (&off)[2][2]) const {
;         const int cume = tab[8 + u.e], cnte = tab[u.e];
; #pragma unroll
;         for (int h = 0; h < 2; ++h)
; #pragma unroll
;             for (int i = 0; i < 2; ++i) {
;                 if (GATHER_) { const int rl = (u.pm - cume) * BM + h * HALF + Rr[i]; const int tok = (rl < cnte) ? idx[u.e * ECAP + rl] : 0; off[h][i] = (unsigned)(tok * KB + Cc[i] * 2); }
;                 else off[h][i] = (unsigned)((u.pm * BM + h * HALF + Rr[i]) * KB + Cc[i] * 2);
;             }
.LBB0_2288:
	s_or_b64 exec, exec, s[8:9]
	v_add_u32_e32 v9, v9, v163
	v_cmp_lt_i32_e32 vcc, v9, v4
	s_and_saveexec_b64 s[8:9], vcc
	s_cbranch_execz .LBB0_2290
	v_lshl_add_u32 v10, v172, 14, v9
	v_ashrrev_i32_e32 v11, 31, v10
	v_lshl_add_u64 v[10:11], v[10:11], 2, s[30:31]
	global_load_dword v7, v[10:11], off

;     __device__ __forceinline__ bool next(int i, Unit& u) const { u.e = 0; return static_next(i, G, c, nM, nN, u.pm, u.pn); }
; template <class Epi, class Sched, bool ALIGN_EPI, int DT>
; __device__ __forceinline__ void gemm_phase(LAS unsigned char* lds, const int KB, const Sched& S, const Epi& E) {
;     ...
;         const bool has_next = S.next(ui + 1, nxt);
;         if constexpr (Sched::GATHER) {
;             if (has_next) S.a_offsets(nxt, Rr, Cc, nxtA);
;             else {
; #pragma unroll
;                 for (int h = 0; h < 2; ++h)
; #pragma unroll
;                     for (int i = 0; i < 2; ++i) nxtA[h][i] = curA[h][i]; }
;         } else nA = has_next ? Ab + (size_t)nxt.pm * 2 * hstep : cA;
;         const char* nB = has_next ? S.b_base(nxt) : cB;
;     ...
; #pragma unroll
;         for (int a = 0; a < 2; ++a)
; #pragma unroll
;             for (int b = 0; b < 2; ++b)
; #pragma unroll
;                 for (int m = 0; m < 4; ++m)
; #pragma unroll
;                     for (int n = 0; n < 2; ++n) acc[a][b][m][n] = (f32x4){0.f, 0.f, 0.f, 0.f};
.LBB0_2291:
	s_and_b64 vcc, exec, s[6:7]
	v_mov_b64_e32 v[154:155], v[2:3]
	s_cbranch_vccnz .LBB0_2293
	s_ashr_i32 s37, s36, 31
	s_lshl_b64 s[8:9], s[36:37], 19
	s_add_u32 s8, s4, s8
	v_mul_hi_i32 v51, v172, s39
	v_mul_lo_u32 v50, v172, s39
	s_addc_u32 s9, s5, s9
	v_lshl_add_u64 v[154:155], s[8:9], 0, v[50:51]
.LBB0_2293:
	v_mov_b32_e32 v79, v147
	v_mov_b32_e32 v87, v147
	v_mov_b32_e32 v50, 0
	v_lshl_add_u64 v[88:89], v[2:3], 0, s[34:35]
	v_lshl_add_u64 v[138:139], s[22:23], 0, v[86:87]
	v_lshl_add_u64 v[140:141], s[22:23], 0, v[78:79]
	s_mov_b32 s37, -2
	s_mov_b64 s[8:9], 0
	v_mov_b32_e32 v51, v50
	v_mov_b32_e32 v52, v50
	v_mov_b32_e32 v53, v50
	v_mov_b32_e32 v54, v50
	v_mov_b32_e32 v55, v50
	v_mov_b32_e32 v56, v50
	v_mov_b32_e32 v57, v50
	v_mov_b32_e32 v66, v50
	v_mov_b32_e32 v67, v50
	v_mov_b32_e32 v68, v50
	v_mov_b32_e32 v69, v50
	v_mov_b32_e32 v74, v50
	v_mov_b32_e32 v75, v50
	v_mov_b32_e32 v76, v50
	v_mov_b32_e32 v77, v50
	v_mov_b32_e32 v90, v50
	v_mov_b32_e32 v91, v50
	v_mov_b32_e32 v92, v50
	v_mov_b32_e32 v93, v50
	v_mov_b32_e32 v98, v50
	v_mov_b32_e32 v99, v50
	v_mov_b32_e32 v100, v50
	v_mov_b32_e32 v101, v50
	v_mov_b32_e32 v106, v50
	v_mov_b32_e32 v107, v50
	v_mov_b32_e32 v108, v50
	v_mov_b32_e32 v109, v50
	v_mov_b32_e32 v114, v50
	v_mov_b32_e32 v115, v50
	v_mov_b32_e32 v116, v50
	v_mov_b32_e32 v117, v50
	v_mov_b32_e32 v122, v50
	v_mov_b32_e32 v123, v50
	v_mov_b32_e32 v124, v50
	v_mov_b32_e32 v125, v50
	v_mov_b32_e32 v130, v50
	v_mov_b32_e32 v131, v50
	v_mov_b32_e32 v132, v50
	v_mov_b32_e32 v133, v50
	v_mov_b32_e32 v70, v50
	v_mov_b32_e32 v71, v50
	v_mov_b32_e32 v72, v50
	v_mov_b32_e32 v73, v50
	v_mov_b32_e32 v82, v50
	v_mov_b32_e32 v83, v50
	v_mov_b32_e32 v84, v50
	v_mov_b32_e32 v85, v50
	v_mov_b32_e32 v94, v50
	v_mov_b32_e32 v95, v50
	v_mov_b32_e32 v96, v50
	v_mov_b32_e32 v97, v50
	v_mov_b32_e32 v102, v50
	v_mov_b32_e32 v103, v50
	v_mov_b32_e32 v104, v50
	v_mov_b32_e32 v105, v50
	v_mov_b32_e32 v110, v50
	v_mov_b32_e32 v111, v50
	v_mov_b32_e32 v112, v50
	v_mov_b32_e32 v113, v50
	v_mov_b32_e32 v118, v50
	v_mov_b32_e32 v119, v50
	v_mov_b32_e32 v120, v50
	v_mov_b32_e32 v121, v50
	v_mov_b32_e32 v126, v50
	v_mov_b32_e32 v127, v50
	v_mov_b32_e32 v128, v50
	v_mov_b32_e32 v129, v50
	v_mov_b32_e32 v134, v50
	v_mov_b32_e32 v135, v50
	v_mov_b32_e32 v136, v50
	v_mov_b32_e32 v137, v50
	v_mov_b32_e32 v42, v50
	v_mov_b32_e32 v43, v50
	v_mov_b32_e32 v44, v50
	v_mov_b32_e32 v45, v50
	v_mov_b32_e32 v34, v50
	v_mov_b32_e32 v35, v50
	v_mov_b32_e32 v36, v50
	v_mov_b32_e32 v37, v50
	v_mov_b32_e32 v26, v50
	v_mov_b32_e32 v27, v50
	v_mov_b32_e32 v28, v50
	v_mov_b32_e32 v29, v50
	v_mov_b32_e32 v18, v50
	v_mov_b32_e32 v19, v50
	v_mov_b32_e32 v20, v50
	v_mov_b32_e32 v21, v50
	v_mov_b32_e32 v10, v50
	v_mov_b32_e32 v11, v50
	v_mov_b32_e32 v12, v50
	v_mov_b32_e32 v13, v50
	v_mov_b32_e32 v2, v50
	v_mov_b32_e32 v3, v50
	s_and_b64 vcc, exec, s[6:7]
	s_cbranch_vccnz .Lgq_skip
	s_waitcnt vmcnt(0)
	v_lshlrev_b32_e32 v5, 11, v5
	v_lshlrev_b32_e32 v6, 11, v6
	v_lshlrev_b32_e32 v8, 11, v8
	v_lshlrev_b32_e32 v7, 11, v7
	v_or_b32_e32 v175, v8, v164
	v_or_b32_e32 v174, v6, v164
	v_or_b32_e32 v173, v5, v164
	v_or_b32_e32 v176, v7, v164
.Lgq_skip:
	v_mov_b32_e32 v4, v50
	v_mov_b32_e32 v5, v50
	v_mov_b32_e32 v62, v50
	v_mov_b32_e32 v63, v50
	v_mov_b32_e32 v64, v50
	v_mov_b32_e32 v65, v50
	v_mov_b32_e32 v58, v50
	v_mov_b32_e32 v59, v50
	v_mov_b32_e32 v60, v50
	v_mov_b32_e32 v61, v50
	v_mov_b32_e32 v46, v50
	v_mov_b32_e32 v47, v50
	v_mov_b32_e32 v48, v50
	v_mov_b32_e32 v49, v50
	v_mov_b32_e32 v38, v50
	v_mov_b32_e32 v39, v50
	v_mov_b32_e32 v40, v50
	v_mov_b32_e32 v41, v50
	v_mov_b32_e32 v30, v50
	v_mov_b32_e32 v31, v50
	v_mov_b32_e32 v32, v50
	v_mov_b32_e32 v33, v50
	v_mov_b32_e32 v22, v50
	v_mov_b32_e32 v23, v50
	v_mov_b32_e32 v24, v50
	v_mov_b32_e32 v25, v50
	v_mov_b32_e32 v14, v50
	v_mov_b32_e32 v15, v50
	v_mov_b32_e32 v16, v50
	v_mov_b32_e32 v17, v50
	v_mov_b32_e32 v6, v50
	v_mov_b32_e32 v7, v50
	v_mov_b32_e32 v8, v50
	v_mov_b32_e32 v9, v50
